# P7 tile-prefix: the 16 per-workgroup expert-count loads issued together, one wait (was 16 load/wait round trips in lockstep)
# baseline (speedup 1.0000x reference)
.LBB0_1092:
	s_or_b64 exec, exec, s[4:5]
	v_readlane_b32 s4, v251, 19
	s_add_i32 s4, s4, 15
	s_ashr_i32 s8, s4, 4
	v_and_b32_e32 v5, 31, v2
	s_cmp_lt_i32 s8, 1
	v_mov_b32_e32 v6, 0
	v_readlane_b32 s5, v251, 20
	s_cbranch_scc1 .LBB0_1097
	v_readlane_b32 s4, v251, 10
	v_ashrrev_i32_e32 v1, 5, v0
	v_readlane_b32 s6, v251, 12
	v_mul_lo_u32 v7, v1, s8
	v_readlane_b32 s5, v251, 11
	v_readlane_b32 s7, v251, 13
	s_add_u32 s4, s6, 0x65d00000
	s_addc_u32 s5, s7, 0
	v_lshl_or_b32 v2, v7, 5, v5
	v_mov_b32_e32 v1, 0
	v_mov_b32_e32 v6, 0
	v_readlane_b32 s10, v251, 19
	v_readlane_b32 s11, v251, 0
	v_mov_b32_e32 v32, 0
	v_mov_b32_e32 v33, 0
	v_mov_b32_e32 v34, 0
	v_mov_b32_e32 v35, 0
	v_mov_b32_e32 v36, 0
	v_mov_b32_e32 v37, 0
	v_mov_b32_e32 v38, 0
	v_mov_b32_e32 v39, 0
	v_mov_b32_e32 v40, 0
	v_mov_b32_e32 v41, 0
	v_mov_b32_e32 v42, 0
	v_mov_b32_e32 v43, 0
	v_mov_b32_e32 v44, 0
	v_mov_b32_e32 v45, 0
	v_mov_b32_e32 v46, 0
	v_mov_b32_e32 v47, 0
	v_mov_b32_e32 v49, 0
	s_cmp_gt_i32 s8, 0
	s_cbranch_scc0 .Lp7_issued
	v_add_u32_e32 v50, 0, v7
	v_cmp_gt_i32_e32 vcc, s10, v50
	s_and_saveexec_b64 s[6:7], vcc
	v_add_u32_e32 v48, 0, v2
	v_lshl_add_u64 v[12:13], v[48:49], 2, s[4:5]
	global_load_dword v32, v[12:13], off
	s_or_b64 exec, exec, s[6:7]
	s_cmp_gt_i32 s8, 1
	s_cbranch_scc0 .Lp7_issued
	v_add_u32_e32 v50, 1, v7
	v_cmp_gt_i32_e32 vcc, s10, v50
	s_and_saveexec_b64 s[6:7], vcc
	v_add_u32_e32 v48, 32, v2
	v_lshl_add_u64 v[12:13], v[48:49], 2, s[4:5]
	global_load_dword v33, v[12:13], off
	s_or_b64 exec, exec, s[6:7]
	s_cmp_gt_i32 s8, 2
	s_cbranch_scc0 .Lp7_issued
	v_add_u32_e32 v50, 2, v7
	v_cmp_gt_i32_e32 vcc, s10, v50
	s_and_saveexec_b64 s[6:7], vcc
	v_add_u32_e32 v48, 64, v2
	v_lshl_add_u64 v[12:13], v[48:49], 2, s[4:5]
	global_load_dword v34, v[12:13], off
	s_or_b64 exec, exec, s[6:7]
	s_cmp_gt_i32 s8, 3
	s_cbranch_scc0 .Lp7_issued
	v_add_u32_e32 v50, 3, v7
	v_cmp_gt_i32_e32 vcc, s10, v50
	s_and_saveexec_b64 s[6:7], vcc
	v_add_u32_e32 v48, 96, v2
	v_lshl_add_u64 v[12:13], v[48:49], 2, s[4:5]
	global_load_dword v35, v[12:13], off
	s_or_b64 exec, exec, s[6:7]
	s_cmp_gt_i32 s8, 4
	s_cbranch_scc0 .Lp7_issued
	v_add_u32_e32 v50, 4, v7
	v_cmp_gt_i32_e32 vcc, s10, v50
	s_and_saveexec_b64 s[6:7], vcc
	v_add_u32_e32 v48, 128, v2
	v_lshl_add_u64 v[12:13], v[48:49], 2, s[4:5]
	global_load_dword v36, v[12:13], off
	s_or_b64 exec, exec, s[6:7]
	s_cmp_gt_i32 s8, 5
	s_cbranch_scc0 .Lp7_issued
	v_add_u32_e32 v50, 5, v7
	v_cmp_gt_i32_e32 vcc, s10, v50
	s_and_saveexec_b64 s[6:7], vcc
	v_add_u32_e32 v48, 160, v2
	v_lshl_add_u64 v[12:13], v[48:49], 2, s[4:5]
	global_load_dword v37, v[12:13], off
	s_or_b64 exec, exec, s[6:7]
	s_cmp_gt_i32 s8, 6
	s_cbranch_scc0 .Lp7_issued
	v_add_u32_e32 v50, 6, v7
	v_cmp_gt_i32_e32 vcc, s10, v50
	s_and_saveexec_b64 s[6:7], vcc
	v_add_u32_e32 v48, 192, v2
	v_lshl_add_u64 v[12:13], v[48:49], 2, s[4:5]
	global_load_dword v38, v[12:13], off
	s_or_b64 exec, exec, s[6:7]
	s_cmp_gt_i32 s8, 7
	s_cbranch_scc0 .Lp7_issued
	v_add_u32_e32 v50, 7, v7
	v_cmp_gt_i32_e32 vcc, s10, v50
	s_and_saveexec_b64 s[6:7], vcc
	v_add_u32_e32 v48, 224, v2
	v_lshl_add_u64 v[12:13], v[48:49], 2, s[4:5]
	global_load_dword v39, v[12:13], off
	s_or_b64 exec, exec, s[6:7]
	s_cmp_gt_i32 s8, 8
	s_cbranch_scc0 .Lp7_issued
	v_add_u32_e32 v50, 8, v7
	v_cmp_gt_i32_e32 vcc, s10, v50
	s_and_saveexec_b64 s[6:7], vcc
	v_add_u32_e32 v48, 256, v2
	v_lshl_add_u64 v[12:13], v[48:49], 2, s[4:5]
	global_load_dword v40, v[12:13], off
	s_or_b64 exec, exec, s[6:7]
	s_cmp_gt_i32 s8, 9
	s_cbranch_scc0 .Lp7_issued
	v_add_u32_e32 v50, 9, v7
	v_cmp_gt_i32_e32 vcc, s10, v50
	s_and_saveexec_b64 s[6:7], vcc
	v_add_u32_e32 v48, 288, v2
	v_lshl_add_u64 v[12:13], v[48:49], 2, s[4:5]
	global_load_dword v41, v[12:13], off
	s_or_b64 exec, exec, s[6:7]
	s_cmp_gt_i32 s8, 10
	s_cbranch_scc0 .Lp7_issued
	v_add_u32_e32 v50, 10, v7
	v_cmp_gt_i32_e32 vcc, s10, v50
	s_and_saveexec_b64 s[6:7], vcc
	v_add_u32_e32 v48, 320, v2
	v_lshl_add_u64 v[12:13], v[48:49], 2, s[4:5]
	global_load_dword v42, v[12:13], off
	s_or_b64 exec, exec, s[6:7]
	s_cmp_gt_i32 s8, 11
	s_cbranch_scc0 .Lp7_issued
	v_add_u32_e32 v50, 11, v7
	v_cmp_gt_i32_e32 vcc, s10, v50
	s_and_saveexec_b64 s[6:7], vcc
	v_add_u32_e32 v48, 352, v2
	v_lshl_add_u64 v[12:13], v[48:49], 2, s[4:5]
	global_load_dword v43, v[12:13], off
	s_or_b64 exec, exec, s[6:7]
	s_cmp_gt_i32 s8, 12
	s_cbranch_scc0 .Lp7_issued
	v_add_u32_e32 v50, 12, v7
	v_cmp_gt_i32_e32 vcc, s10, v50
	s_and_saveexec_b64 s[6:7], vcc
	v_add_u32_e32 v48, 384, v2
	v_lshl_add_u64 v[12:13], v[48:49], 2, s[4:5]
	global_load_dword v44, v[12:13], off
	s_or_b64 exec, exec, s[6:7]
	s_cmp_gt_i32 s8, 13
	s_cbranch_scc0 .Lp7_issued
	v_add_u32_e32 v50, 13, v7
	v_cmp_gt_i32_e32 vcc, s10, v50
	s_and_saveexec_b64 s[6:7], vcc
	v_add_u32_e32 v48, 416, v2
	v_lshl_add_u64 v[12:13], v[48:49], 2, s[4:5]
	global_load_dword v45, v[12:13], off
	s_or_b64 exec, exec, s[6:7]
	s_cmp_gt_i32 s8, 14
	s_cbranch_scc0 .Lp7_issued
	v_add_u32_e32 v50, 14, v7
	v_cmp_gt_i32_e32 vcc, s10, v50
	s_and_saveexec_b64 s[6:7], vcc
	v_add_u32_e32 v48, 448, v2
	v_lshl_add_u64 v[12:13], v[48:49], 2, s[4:5]
	global_load_dword v46, v[12:13], off
	s_or_b64 exec, exec, s[6:7]
	s_cmp_gt_i32 s8, 15
	s_cbranch_scc0 .Lp7_issued
	v_add_u32_e32 v50, 15, v7
	v_cmp_gt_i32_e32 vcc, s10, v50
	s_and_saveexec_b64 s[6:7], vcc
	v_add_u32_e32 v48, 480, v2
	v_lshl_add_u64 v[12:13], v[48:49], 2, s[4:5]
	global_load_dword v47, v[12:13], off
	s_or_b64 exec, exec, s[6:7]
.Lp7_issued:
	s_waitcnt vmcnt(0)
	v_add_u32_e32 v50, 0, v7
	v_add_u32_e32 v1, v32, v1
	v_cmp_gt_i32_e32 vcc, s11, v50
	v_cndmask_b32_e32 v51, 0, v32, vcc
	v_add_u32_e32 v6, v51, v6
	v_add_u32_e32 v50, 1, v7
	v_add_u32_e32 v1, v33, v1
	v_cmp_gt_i32_e32 vcc, s11, v50
	v_cndmask_b32_e32 v51, 0, v33, vcc
	v_add_u32_e32 v6, v51, v6
	v_add_u32_e32 v50, 2, v7
	v_add_u32_e32 v1, v34, v1
	v_cmp_gt_i32_e32 vcc, s11, v50
	v_cndmask_b32_e32 v51, 0, v34, vcc
	v_add_u32_e32 v6, v51, v6
	v_add_u32_e32 v50, 3, v7
	v_add_u32_e32 v1, v35, v1
	v_cmp_gt_i32_e32 vcc, s11, v50
	v_cndmask_b32_e32 v51, 0, v35, vcc
	v_add_u32_e32 v6, v51, v6
	v_add_u32_e32 v50, 4, v7
	v_add_u32_e32 v1, v36, v1
	v_cmp_gt_i32_e32 vcc, s11, v50
	v_cndmask_b32_e32 v51, 0, v36, vcc
	v_add_u32_e32 v6, v51, v6
	v_add_u32_e32 v50, 5, v7
	v_add_u32_e32 v1, v37, v1
	v_cmp_gt_i32_e32 vcc, s11, v50
	v_cndmask_b32_e32 v51, 0, v37, vcc
	v_add_u32_e32 v6, v51, v6
	v_add_u32_e32 v50, 6, v7
	v_add_u32_e32 v1, v38, v1
	v_cmp_gt_i32_e32 vcc, s11, v50
	v_cndmask_b32_e32 v51, 0, v38, vcc
	v_add_u32_e32 v6, v51, v6
	v_add_u32_e32 v50, 7, v7
	v_add_u32_e32 v1, v39, v1
	v_cmp_gt_i32_e32 vcc, s11, v50
	v_cndmask_b32_e32 v51, 0, v39, vcc
	v_add_u32_e32 v6, v51, v6
	v_add_u32_e32 v50, 8, v7
	v_add_u32_e32 v1, v40, v1
	v_cmp_gt_i32_e32 vcc, s11, v50
	v_cndmask_b32_e32 v51, 0, v40, vcc
	v_add_u32_e32 v6, v51, v6
	v_add_u32_e32 v50, 9, v7
	v_add_u32_e32 v1, v41, v1
	v_cmp_gt_i32_e32 vcc, s11, v50
	v_cndmask_b32_e32 v51, 0, v41, vcc
	v_add_u32_e32 v6, v51, v6
	v_add_u32_e32 v50, 10, v7
	v_add_u32_e32 v1, v42, v1
	v_cmp_gt_i32_e32 vcc, s11, v50
	v_cndmask_b32_e32 v51, 0, v42, vcc
	v_add_u32_e32 v6, v51, v6
	v_add_u32_e32 v50, 11, v7
	v_add_u32_e32 v1, v43, v1
	v_cmp_gt_i32_e32 vcc, s11, v50
	v_cndmask_b32_e32 v51, 0, v43, vcc
	v_add_u32_e32 v6, v51, v6
	v_add_u32_e32 v50, 12, v7
	v_add_u32_e32 v1, v44, v1
	v_cmp_gt_i32_e32 vcc, s11, v50
	v_cndmask_b32_e32 v51, 0, v44, vcc
	v_add_u32_e32 v6, v51, v6
	v_add_u32_e32 v50, 13, v7
	v_add_u32_e32 v1, v45, v1
	v_cmp_gt_i32_e32 vcc, s11, v50
	v_cndmask_b32_e32 v51, 0, v45, vcc
	v_add_u32_e32 v6, v51, v6
	v_add_u32_e32 v50, 14, v7
	v_add_u32_e32 v1, v46, v1
	v_cmp_gt_i32_e32 vcc, s11, v50
	v_cndmask_b32_e32 v51, 0, v46, vcc
	v_add_u32_e32 v6, v51, v6
	v_add_u32_e32 v50, 15, v7
	v_add_u32_e32 v1, v47, v1
	v_cmp_gt_i32_e32 vcc, s11, v50
	v_cndmask_b32_e32 v51, 0, v47, vcc
	v_add_u32_e32 v6, v51, v6
